# union 2: adds the out-projection epilogue with residual loads in flight and the up-projection epilogue with load-before-store order
# baseline (speedup 1.0000x reference)
.LBB0_679:
	v_mov_b32_e32 v130, v166
	v_mov_b32_e32 v131, v1
	s_nop 15
	s_nop 15
	v_mov_b64_e32 v[134:135], s[8:9]
	v_lshl_add_u32 v130, v130, 3, s58
	v_add_u32_e32 v132, s57, v131
	v_ashrrev_i32_e32 v131, 31, v130
	v_mad_i64_i32 v[158:159], s[24:25], v132, s50, v[134:135]
	v_lshlrev_b64 v[136:137], 1, v[130:131]
	v_lshl_add_u64 v[162:163], v[158:159], 0, v[136:137]
	v_add_co_u32_e32 v158, vcc, s44, v162
	v_ashrrev_i32_e32 v133, 31, v132
	s_nop 0
	v_addc_co_u32_e32 v159, vcc, 0, v163, vcc
	global_load_dwordx4 v[158:161], v[158:159], off offset:3072
	v_lshlrev_b64 v[172:173], 11, v[132:133]
	v_mov_b32_e32 v164, 0
	v_mov_b32_e32 v165, 0
	s_waitcnt vmcnt(0)
	v_lshlrev_b32_e32 v133, 16, v158
	v_and_b32_e32 v158, 0xffff0000, v158
	v_lshlrev_b32_e32 v174, 16, v160
	v_and_b32_e32 v160, 0xffff0000, v160
	v_lshlrev_b32_e32 v171, 16, v159
	v_and_b32_e32 v159, 0xffff0000, v159
	v_lshlrev_b32_e32 v175, 16, v161
	v_and_b32_e32 v161, 0xffff0000, v161
	v_max_f32_e32 v133, v133, v133
	v_max_f32_e32 v174, v174, v174
	v_max_f32_e32 v176, v158, v158
	v_max_f32_e32 v177, v160, v160
	v_max_f32_e32 v178, v159, v159
	v_max_f32_e32 v179, v161, v161
	v_max_f32_e32 v158, 0xda24260, v133
	v_max_f32_e32 v160, 0xda24260, v174
	v_max_f32_e32 v159, 0xda24260, v176
	v_max_f32_e32 v161, 0xda24260, v177
	v_pk_mul_f32 v[126:127], v[126:127], v[158:159]
	v_pk_mul_f32 v[122:123], v[122:123], v[160:161]
	v_pk_mul_f32 v[126:127], v[126:127], s[20:21] op_sel_hi:[1,0]
	v_pk_mul_f32 v[122:123], v[122:123], s[20:21] op_sel_hi:[1,0]
	v_max_f32_e32 v171, v171, v171
	v_max_f32_e32 v175, v175, v175
	v_med3_f32 v126, v126, s54, v170
	v_med3_f32 v122, v122, s54, v170
	v_med3_f32 v127, v127, s54, v170
	v_med3_f32 v123, v123, s54, v170
	v_max_f32_e32 v174, 0xda24260, v171
	v_max_f32_e32 v176, 0xda24260, v175
	v_max_f32_e32 v175, 0xda24260, v178
	v_max_f32_e32 v177, 0xda24260, v179
	v_cvt_pk_fp8_f32 v164, v126, v127
	v_cvt_pk_fp8_f32 v165, v122, v123
	v_pk_mul_f32 v[128:129], v[128:129], v[174:175]
	v_pk_mul_f32 v[124:125], v[124:125], v[176:177]
	v_pk_mul_f32 v[128:129], v[128:129], s[20:21] op_sel_hi:[1,0]
	v_pk_mul_f32 v[124:125], v[124:125], s[20:21] op_sel_hi:[1,0]
	v_med3_f32 v128, v128, s54, v170
	v_med3_f32 v124, v124, s54, v170
	v_med3_f32 v122, v129, s54, v170
	v_med3_f32 v123, v125, s54, v170
	v_cvt_pk_fp8_f32 v164, v128, v122 op_sel:[0,0,1]
	v_cvt_pk_fp8_f32 v165, v124, v123 op_sel:[0,0,1]
	v_lshl_add_u64 v[122:123], s[10:11], 0, v[172:173]
	v_lshl_add_u64 v[126:127], v[122:123], 0, v[130:131]
	v_lshl_add_u64 v[124:125], v[162:163], 0, s[18:19]
	global_load_dwordx4 v[122:125], v[124:125], off offset:256
	global_store_dwordx2 v[126:127], v[164:165], off
	v_mov_b32_e32 v128, 0
	v_mov_b32_e32 v129, 0
	v_add_u32_e32 v158, 16, v132
	v_mad_i64_i32 v[160:161], s[24:25], v158, s50, v[134:135]
	v_lshl_add_u64 v[160:161], v[160:161], 0, v[136:137]
	s_waitcnt vmcnt(1)
	v_lshlrev_b32_e32 v133, 16, v122
	v_and_b32_e32 v122, 0xffff0000, v122
	v_lshlrev_b32_e32 v162, 16, v124
	v_and_b32_e32 v124, 0xffff0000, v124
	v_lshlrev_b32_e32 v159, 16, v123
	v_and_b32_e32 v123, 0xffff0000, v123
	v_lshlrev_b32_e32 v163, 16, v125
	v_and_b32_e32 v125, 0xffff0000, v125
	v_max_f32_e32 v133, v133, v133
	v_max_f32_e32 v162, v162, v162
	v_max_f32_e32 v164, v122, v122
	v_max_f32_e32 v165, v124, v124
	v_max_f32_e32 v171, v123, v123
	v_max_f32_e32 v172, v125, v125
	v_max_f32_e32 v122, 0xda24260, v133
	v_max_f32_e32 v124, 0xda24260, v162
	v_max_f32_e32 v123, 0xda24260, v164
	v_max_f32_e32 v125, 0xda24260, v165
	v_pk_mul_f32 v[118:119], v[118:119], v[122:123]
	v_pk_mul_f32 v[114:115], v[114:115], v[124:125]
	v_pk_mul_f32 v[118:119], v[118:119], s[20:21] op_sel_hi:[1,0]
	v_pk_mul_f32 v[114:115], v[114:115], s[20:21] op_sel_hi:[1,0]
	v_max_f32_e32 v159, v159, v159
	v_max_f32_e32 v163, v163, v163
	v_med3_f32 v118, v118, s54, v170
	v_med3_f32 v114, v114, s54, v170
	v_med3_f32 v119, v119, s54, v170
	v_med3_f32 v115, v115, s54, v170
	v_max_f32_e32 v162, 0xda24260, v159
	v_max_f32_e32 v164, 0xda24260, v163
	v_max_f32_e32 v163, 0xda24260, v171
	v_max_f32_e32 v165, 0xda24260, v172
	v_cvt_pk_fp8_f32 v128, v118, v119
	v_cvt_pk_fp8_f32 v129, v114, v115
	v_pk_mul_f32 v[120:121], v[120:121], v[162:163]
	v_pk_mul_f32 v[116:117], v[116:117], v[164:165]
	v_pk_mul_f32 v[120:121], v[120:121], s[20:21] op_sel_hi:[1,0]
	v_pk_mul_f32 v[116:117], v[116:117], s[20:21] op_sel_hi:[1,0]
	v_med3_f32 v120, v120, s54, v170
	v_med3_f32 v116, v116, s54, v170
	v_med3_f32 v114, v121, s54, v170
	v_med3_f32 v115, v117, s54, v170
	v_cvt_pk_fp8_f32 v128, v120, v114 op_sel:[0,0,1]
	v_cvt_pk_fp8_f32 v129, v116, v115 op_sel:[0,0,1]
	v_add_co_u32_e32 v114, vcc, s44, v160
	v_mov_b32_e32 v118, 0
	s_nop 0
	v_addc_co_u32_e32 v115, vcc, 0, v161, vcc
	global_load_dwordx4 v[114:117], v[114:115], off offset:3072
	global_store_dwordx2 v[126:127], v[128:129], off offset:128
	v_mov_b32_e32 v119, 0
	v_ashrrev_i32_e32 v159, 31, v158
	v_lshlrev_b64 v[120:121], 11, v[158:159]
	s_waitcnt vmcnt(1)
	v_lshlrev_b32_e32 v122, 16, v114
	v_and_b32_e32 v114, 0xffff0000, v114
	v_lshlrev_b32_e32 v124, 16, v116
	v_and_b32_e32 v116, 0xffff0000, v116
	v_lshlrev_b32_e32 v123, 16, v115
	v_and_b32_e32 v115, 0xffff0000, v115
	v_lshlrev_b32_e32 v125, 16, v117
	v_and_b32_e32 v117, 0xffff0000, v117
	v_max_f32_e32 v122, v122, v122
	v_max_f32_e32 v124, v124, v124
	v_max_f32_e32 v126, v114, v114
	v_max_f32_e32 v127, v116, v116
	v_max_f32_e32 v128, v115, v115
	v_max_f32_e32 v129, v117, v117
	v_max_f32_e32 v114, 0xda24260, v122
	v_max_f32_e32 v116, 0xda24260, v124
	v_max_f32_e32 v115, 0xda24260, v126
	v_max_f32_e32 v117, 0xda24260, v127
	v_pk_mul_f32 v[110:111], v[110:111], v[114:115]
	v_pk_mul_f32 v[106:107], v[106:107], v[116:117]
	v_pk_mul_f32 v[110:111], v[110:111], s[20:21] op_sel_hi:[1,0]
	v_pk_mul_f32 v[106:107], v[106:107], s[20:21] op_sel_hi:[1,0]
	v_max_f32_e32 v123, v123, v123
	v_max_f32_e32 v125, v125, v125
	v_med3_f32 v110, v110, s54, v170
	v_med3_f32 v106, v106, s54, v170
	v_med3_f32 v111, v111, s54, v170
	v_med3_f32 v107, v107, s54, v170
	v_max_f32_e32 v122, 0xda24260, v123
	v_max_f32_e32 v124, 0xda24260, v125
	v_max_f32_e32 v123, 0xda24260, v128
	v_max_f32_e32 v125, 0xda24260, v129
	v_cvt_pk_fp8_f32 v118, v110, v111
	v_cvt_pk_fp8_f32 v119, v106, v107
	v_pk_mul_f32 v[112:113], v[112:113], v[122:123]
	v_pk_mul_f32 v[108:109], v[108:109], v[124:125]
	v_pk_mul_f32 v[112:113], v[112:113], s[20:21] op_sel_hi:[1,0]
	v_pk_mul_f32 v[108:109], v[108:109], s[20:21] op_sel_hi:[1,0]
	v_med3_f32 v112, v112, s54, v170
	v_med3_f32 v108, v108, s54, v170
	v_med3_f32 v106, v113, s54, v170
	v_med3_f32 v107, v109, s54, v170
	v_cvt_pk_fp8_f32 v118, v112, v106 op_sel:[0,0,1]
	v_cvt_pk_fp8_f32 v119, v108, v107 op_sel:[0,0,1]
	v_lshl_add_u64 v[108:109], s[10:11], 0, v[120:121]
	v_lshl_add_u64 v[110:111], v[108:109], 0, v[130:131]
	v_lshl_add_u64 v[106:107], v[160:161], 0, s[18:19]
	global_load_dwordx4 v[106:109], v[106:107], off offset:256
	global_store_dwordx2 v[110:111], v[118:119], off
	v_mov_b32_e32 v112, 0
	v_mov_b32_e32 v113, 0
	v_add_u32_e32 v114, 32, v132
	v_mad_i64_i32 v[116:117], s[24:25], v114, s50, v[134:135]
	v_lshl_add_u64 v[116:117], v[116:117], 0, v[136:137]
	s_waitcnt vmcnt(1)
	v_lshlrev_b32_e32 v115, 16, v106
	v_and_b32_e32 v106, 0xffff0000, v106
	v_lshlrev_b32_e32 v119, 16, v108
	v_and_b32_e32 v108, 0xffff0000, v108
	v_lshlrev_b32_e32 v118, 16, v107
	v_and_b32_e32 v107, 0xffff0000, v107
	v_lshlrev_b32_e32 v120, 16, v109
	v_and_b32_e32 v109, 0xffff0000, v109
	v_max_f32_e32 v115, v115, v115
	v_max_f32_e32 v119, v119, v119
	v_max_f32_e32 v121, v106, v106
	v_max_f32_e32 v122, v108, v108
	v_max_f32_e32 v123, v107, v107
	v_max_f32_e32 v124, v109, v109
	v_max_f32_e32 v106, 0xda24260, v115
	v_max_f32_e32 v108, 0xda24260, v119
	v_max_f32_e32 v107, 0xda24260, v121
	v_max_f32_e32 v109, 0xda24260, v122
	v_pk_mul_f32 v[102:103], v[102:103], v[106:107]
	v_pk_mul_f32 v[98:99], v[98:99], v[108:109]
	v_pk_mul_f32 v[102:103], v[102:103], s[20:21] op_sel_hi:[1,0]
	v_pk_mul_f32 v[98:99], v[98:99], s[20:21] op_sel_hi:[1,0]
	v_max_f32_e32 v118, v118, v118
	v_max_f32_e32 v120, v120, v120
	v_med3_f32 v102, v102, s54, v170
	v_med3_f32 v98, v98, s54, v170
	v_med3_f32 v103, v103, s54, v170
	v_med3_f32 v99, v99, s54, v170
	v_max_f32_e32 v118, 0xda24260, v118
	v_max_f32_e32 v120, 0xda24260, v120
	v_max_f32_e32 v119, 0xda24260, v123
	v_max_f32_e32 v121, 0xda24260, v124
	v_cvt_pk_fp8_f32 v112, v102, v103
	v_cvt_pk_fp8_f32 v113, v98, v99
	v_pk_mul_f32 v[104:105], v[104:105], v[118:119]
	v_pk_mul_f32 v[100:101], v[100:101], v[120:121]
	v_pk_mul_f32 v[104:105], v[104:105], s[20:21] op_sel_hi:[1,0]
	v_pk_mul_f32 v[100:101], v[100:101], s[20:21] op_sel_hi:[1,0]
	v_med3_f32 v104, v104, s54, v170
	v_med3_f32 v100, v100, s54, v170
	v_med3_f32 v98, v105, s54, v170
	v_med3_f32 v99, v101, s54, v170
	v_cvt_pk_fp8_f32 v112, v104, v98 op_sel:[0,0,1]
	v_cvt_pk_fp8_f32 v113, v100, v99 op_sel:[0,0,1]
	v_add_co_u32_e32 v98, vcc, s44, v116
	v_mov_b32_e32 v102, 0
	s_nop 0
	v_addc_co_u32_e32 v99, vcc, 0, v117, vcc
	global_load_dwordx4 v[98:101], v[98:99], off offset:3072
	global_store_dwordx2 v[110:111], v[112:113], off offset:128
	v_mov_b32_e32 v103, 0
	v_ashrrev_i32_e32 v115, 31, v114
	v_lshlrev_b64 v[104:105], 11, v[114:115]
	s_waitcnt vmcnt(1)
	v_lshlrev_b32_e32 v106, 16, v98
	v_and_b32_e32 v98, 0xffff0000, v98
	v_lshlrev_b32_e32 v108, 16, v100
	v_and_b32_e32 v100, 0xffff0000, v100
	v_lshlrev_b32_e32 v107, 16, v99
	v_and_b32_e32 v99, 0xffff0000, v99
	v_lshlrev_b32_e32 v109, 16, v101
	v_and_b32_e32 v101, 0xffff0000, v101
	v_max_f32_e32 v106, v106, v106
	v_max_f32_e32 v108, v108, v108
	v_max_f32_e32 v110, v98, v98
	v_max_f32_e32 v111, v100, v100
	v_max_f32_e32 v112, v99, v99
	v_max_f32_e32 v113, v101, v101
	v_max_f32_e32 v98, 0xda24260, v106
	v_max_f32_e32 v100, 0xda24260, v108
	v_max_f32_e32 v99, 0xda24260, v110
	v_max_f32_e32 v101, 0xda24260, v111
	v_pk_mul_f32 v[94:95], v[94:95], v[98:99]
	v_pk_mul_f32 v[90:91], v[90:91], v[100:101]
	v_pk_mul_f32 v[94:95], v[94:95], s[20:21] op_sel_hi:[1,0]
	v_pk_mul_f32 v[90:91], v[90:91], s[20:21] op_sel_hi:[1,0]
	v_max_f32_e32 v107, v107, v107
	v_max_f32_e32 v109, v109, v109
	v_med3_f32 v94, v94, s54, v170
	v_med3_f32 v90, v90, s54, v170
	v_med3_f32 v95, v95, s54, v170
	v_med3_f32 v91, v91, s54, v170
	v_max_f32_e32 v106, 0xda24260, v107
	v_max_f32_e32 v108, 0xda24260, v109
	v_max_f32_e32 v107, 0xda24260, v112
	v_max_f32_e32 v109, 0xda24260, v113
	v_cvt_pk_fp8_f32 v102, v94, v95
	v_cvt_pk_fp8_f32 v103, v90, v91
	v_pk_mul_f32 v[96:97], v[96:97], v[106:107]
	v_pk_mul_f32 v[92:93], v[92:93], v[108:109]
	v_pk_mul_f32 v[96:97], v[96:97], s[20:21] op_sel_hi:[1,0]
	v_pk_mul_f32 v[92:93], v[92:93], s[20:21] op_sel_hi:[1,0]
	v_med3_f32 v96, v96, s54, v170
	v_med3_f32 v92, v92, s54, v170
	v_med3_f32 v90, v97, s54, v170
	v_med3_f32 v91, v93, s54, v170
	v_cvt_pk_fp8_f32 v102, v96, v90 op_sel:[0,0,1]
	v_cvt_pk_fp8_f32 v103, v92, v91 op_sel:[0,0,1]
	v_lshl_add_u64 v[92:93], s[10:11], 0, v[104:105]
	v_lshl_add_u64 v[94:95], v[92:93], 0, v[130:131]
	v_lshl_add_u64 v[90:91], v[116:117], 0, s[18:19]
	global_load_dwordx4 v[90:93], v[90:91], off offset:256
	global_store_dwordx2 v[94:95], v[102:103], off
	v_mov_b32_e32 v96, 0
	v_mov_b32_e32 v97, 0
	v_add_u32_e32 v98, 48, v132
	v_mad_i64_i32 v[100:101], s[24:25], v98, s50, v[134:135]
	v_lshl_add_u64 v[100:101], v[100:101], 0, v[136:137]
	s_waitcnt vmcnt(1)
	v_lshlrev_b32_e32 v99, 16, v90
	v_and_b32_e32 v90, 0xffff0000, v90
	v_lshlrev_b32_e32 v103, 16, v92
	v_and_b32_e32 v92, 0xffff0000, v92
	v_lshlrev_b32_e32 v102, 16, v91
	v_and_b32_e32 v91, 0xffff0000, v91
	v_lshlrev_b32_e32 v104, 16, v93
	v_and_b32_e32 v93, 0xffff0000, v93
	v_max_f32_e32 v99, v99, v99
	v_max_f32_e32 v103, v103, v103
	v_max_f32_e32 v105, v90, v90
	v_max_f32_e32 v106, v92, v92
	v_max_f32_e32 v107, v91, v91
	v_max_f32_e32 v108, v93, v93
	v_max_f32_e32 v90, 0xda24260, v99
	v_max_f32_e32 v92, 0xda24260, v103
	v_max_f32_e32 v91, 0xda24260, v105
	v_max_f32_e32 v93, 0xda24260, v106
	v_pk_mul_f32 v[86:87], v[86:87], v[90:91]
	v_pk_mul_f32 v[82:83], v[82:83], v[92:93]
	v_pk_mul_f32 v[86:87], v[86:87], s[20:21] op_sel_hi:[1,0]
	v_pk_mul_f32 v[82:83], v[82:83], s[20:21] op_sel_hi:[1,0]
	v_max_f32_e32 v102, v102, v102
	v_max_f32_e32 v104, v104, v104
	v_med3_f32 v86, v86, s54, v170
	v_med3_f32 v82, v82, s54, v170
	v_med3_f32 v87, v87, s54, v170
	v_med3_f32 v83, v83, s54, v170
	v_max_f32_e32 v102, 0xda24260, v102
	v_max_f32_e32 v104, 0xda24260, v104
	v_max_f32_e32 v103, 0xda24260, v107
	v_max_f32_e32 v105, 0xda24260, v108
	v_cvt_pk_fp8_f32 v96, v86, v87
	v_cvt_pk_fp8_f32 v97, v82, v83
	v_pk_mul_f32 v[88:89], v[88:89], v[102:103]
	v_pk_mul_f32 v[84:85], v[84:85], v[104:105]
	v_pk_mul_f32 v[88:89], v[88:89], s[20:21] op_sel_hi:[1,0]
	v_pk_mul_f32 v[84:85], v[84:85], s[20:21] op_sel_hi:[1,0]
	v_med3_f32 v88, v88, s54, v170
	v_med3_f32 v84, v84, s54, v170
	v_med3_f32 v82, v89, s54, v170
	v_med3_f32 v83, v85, s54, v170
	v_cvt_pk_fp8_f32 v96, v88, v82 op_sel:[0,0,1]
	v_cvt_pk_fp8_f32 v97, v84, v83 op_sel:[0,0,1]
	v_add_co_u32_e32 v82, vcc, s44, v100
	v_mov_b32_e32 v86, 0
	s_nop 0
	v_addc_co_u32_e32 v83, vcc, 0, v101, vcc
	global_load_dwordx4 v[82:85], v[82:83], off offset:3072
	global_store_dwordx2 v[94:95], v[96:97], off offset:128
	v_mov_b32_e32 v87, 0
	v_ashrrev_i32_e32 v99, 31, v98
	v_lshlrev_b64 v[88:89], 11, v[98:99]
	s_waitcnt vmcnt(1)
	v_lshlrev_b32_e32 v90, 16, v82
	v_and_b32_e32 v82, 0xffff0000, v82
	v_lshlrev_b32_e32 v92, 16, v84
	v_and_b32_e32 v84, 0xffff0000, v84
	v_lshlrev_b32_e32 v91, 16, v83
	v_and_b32_e32 v83, 0xffff0000, v83
	v_lshlrev_b32_e32 v93, 16, v85
	v_and_b32_e32 v85, 0xffff0000, v85
	v_max_f32_e32 v90, v90, v90
	v_max_f32_e32 v92, v92, v92
	v_max_f32_e32 v94, v82, v82
	v_max_f32_e32 v95, v84, v84
	v_max_f32_e32 v96, v83, v83
	v_max_f32_e32 v97, v85, v85
	v_max_f32_e32 v82, 0xda24260, v90
	v_max_f32_e32 v84, 0xda24260, v92
	v_max_f32_e32 v83, 0xda24260, v94
	v_max_f32_e32 v85, 0xda24260, v95
	v_pk_mul_f32 v[78:79], v[78:79], v[82:83]
	v_pk_mul_f32 v[74:75], v[74:75], v[84:85]
	v_pk_mul_f32 v[78:79], v[78:79], s[20:21] op_sel_hi:[1,0]
	v_pk_mul_f32 v[74:75], v[74:75], s[20:21] op_sel_hi:[1,0]
	v_max_f32_e32 v91, v91, v91
	v_max_f32_e32 v93, v93, v93
	v_med3_f32 v78, v78, s54, v170
	v_med3_f32 v74, v74, s54, v170
	v_med3_f32 v79, v79, s54, v170
	v_med3_f32 v75, v75, s54, v170
	v_max_f32_e32 v90, 0xda24260, v91
	v_max_f32_e32 v92, 0xda24260, v93
	v_max_f32_e32 v91, 0xda24260, v96
	v_max_f32_e32 v93, 0xda24260, v97
	v_cvt_pk_fp8_f32 v86, v78, v79
	v_cvt_pk_fp8_f32 v87, v74, v75
	v_pk_mul_f32 v[80:81], v[80:81], v[90:91]
	v_pk_mul_f32 v[76:77], v[76:77], v[92:93]
	v_pk_mul_f32 v[80:81], v[80:81], s[20:21] op_sel_hi:[1,0]
	v_pk_mul_f32 v[76:77], v[76:77], s[20:21] op_sel_hi:[1,0]
	v_med3_f32 v80, v80, s54, v170
	v_med3_f32 v76, v76, s54, v170
	v_med3_f32 v74, v81, s54, v170
	v_med3_f32 v75, v77, s54, v170
	v_cvt_pk_fp8_f32 v86, v80, v74 op_sel:[0,0,1]
	v_cvt_pk_fp8_f32 v87, v76, v75 op_sel:[0,0,1]
	v_lshl_add_u64 v[76:77], s[10:11], 0, v[88:89]
	v_lshl_add_u64 v[78:79], v[76:77], 0, v[130:131]
	v_lshl_add_u64 v[74:75], v[100:101], 0, s[18:19]
	global_load_dwordx4 v[74:77], v[74:75], off offset:256
	global_store_dwordx2 v[78:79], v[86:87], off
	v_mov_b32_e32 v80, 0
	v_mov_b32_e32 v81, 0
	v_add_u32_e32 v82, 0x80, v132
	v_mad_i64_i32 v[84:85], s[24:25], v82, s50, v[134:135]
	v_lshl_add_u64 v[84:85], v[84:85], 0, v[136:137]
	s_waitcnt vmcnt(1)
	v_lshlrev_b32_e32 v83, 16, v74
	v_and_b32_e32 v74, 0xffff0000, v74
	v_lshlrev_b32_e32 v87, 16, v76
	v_and_b32_e32 v76, 0xffff0000, v76
	v_lshlrev_b32_e32 v86, 16, v75
	v_and_b32_e32 v75, 0xffff0000, v75
	v_lshlrev_b32_e32 v88, 16, v77
	v_and_b32_e32 v77, 0xffff0000, v77
	v_max_f32_e32 v83, v83, v83
	v_max_f32_e32 v87, v87, v87
	v_max_f32_e32 v89, v74, v74
	v_max_f32_e32 v90, v76, v76
	v_max_f32_e32 v91, v75, v75
	v_max_f32_e32 v92, v77, v77
	v_max_f32_e32 v74, 0xda24260, v83
	v_max_f32_e32 v76, 0xda24260, v87
	v_max_f32_e32 v75, 0xda24260, v89
	v_max_f32_e32 v77, 0xda24260, v90
	v_pk_mul_f32 v[70:71], v[70:71], v[74:75]
	v_pk_mul_f32 v[66:67], v[66:67], v[76:77]
	v_pk_mul_f32 v[70:71], v[70:71], s[20:21] op_sel_hi:[1,0]
	v_pk_mul_f32 v[66:67], v[66:67], s[20:21] op_sel_hi:[1,0]
	v_max_f32_e32 v86, v86, v86
	v_max_f32_e32 v88, v88, v88
	v_med3_f32 v70, v70, s54, v170
	v_med3_f32 v66, v66, s54, v170
	v_med3_f32 v71, v71, s54, v170
	v_med3_f32 v67, v67, s54, v170
	v_max_f32_e32 v86, 0xda24260, v86
	v_max_f32_e32 v88, 0xda24260, v88
	v_max_f32_e32 v87, 0xda24260, v91
	v_max_f32_e32 v89, 0xda24260, v92
	v_cvt_pk_fp8_f32 v80, v70, v71
	v_cvt_pk_fp8_f32 v81, v66, v67
	v_pk_mul_f32 v[72:73], v[72:73], v[86:87]
	v_pk_mul_f32 v[68:69], v[68:69], v[88:89]
	v_pk_mul_f32 v[72:73], v[72:73], s[20:21] op_sel_hi:[1,0]
	v_pk_mul_f32 v[68:69], v[68:69], s[20:21] op_sel_hi:[1,0]
	v_med3_f32 v72, v72, s54, v170
	v_med3_f32 v68, v68, s54, v170
	v_med3_f32 v66, v73, s54, v170
	v_med3_f32 v67, v69, s54, v170
	v_cvt_pk_fp8_f32 v80, v72, v66 op_sel:[0,0,1]
	v_cvt_pk_fp8_f32 v81, v68, v67 op_sel:[0,0,1]
	v_add_co_u32_e32 v66, vcc, s44, v84
	v_mov_b32_e32 v70, 0
	s_nop 0
	v_addc_co_u32_e32 v67, vcc, 0, v85, vcc
	global_load_dwordx4 v[66:69], v[66:67], off offset:3072
	global_store_dwordx2 v[78:79], v[80:81], off offset:128
	v_mov_b32_e32 v71, 0
	v_ashrrev_i32_e32 v83, 31, v82
	v_lshlrev_b64 v[72:73], 11, v[82:83]
	s_waitcnt vmcnt(1)
	v_lshlrev_b32_e32 v74, 16, v66
	v_and_b32_e32 v66, 0xffff0000, v66
	v_lshlrev_b32_e32 v76, 16, v68
	v_and_b32_e32 v68, 0xffff0000, v68
	v_lshlrev_b32_e32 v75, 16, v67
	v_and_b32_e32 v67, 0xffff0000, v67
	v_lshlrev_b32_e32 v77, 16, v69
	v_and_b32_e32 v69, 0xffff0000, v69
	v_max_f32_e32 v74, v74, v74
	v_max_f32_e32 v76, v76, v76
	v_max_f32_e32 v78, v66, v66
	v_max_f32_e32 v79, v68, v68
	v_max_f32_e32 v80, v67, v67
	v_max_f32_e32 v81, v69, v69
	v_max_f32_e32 v66, 0xda24260, v74
	v_max_f32_e32 v68, 0xda24260, v76
	v_max_f32_e32 v67, 0xda24260, v78
	v_max_f32_e32 v69, 0xda24260, v79
	v_pk_mul_f32 v[62:63], v[62:63], v[66:67]
	v_pk_mul_f32 v[58:59], v[58:59], v[68:69]
	v_pk_mul_f32 v[62:63], v[62:63], s[20:21] op_sel_hi:[1,0]
	v_pk_mul_f32 v[58:59], v[58:59], s[20:21] op_sel_hi:[1,0]
	v_max_f32_e32 v75, v75, v75
	v_max_f32_e32 v77, v77, v77
	v_med3_f32 v62, v62, s54, v170
	v_med3_f32 v58, v58, s54, v170
	v_med3_f32 v63, v63, s54, v170
	v_med3_f32 v59, v59, s54, v170
	v_max_f32_e32 v74, 0xda24260, v75
	v_max_f32_e32 v76, 0xda24260, v77
	v_max_f32_e32 v75, 0xda24260, v80
	v_max_f32_e32 v77, 0xda24260, v81
	v_cvt_pk_fp8_f32 v70, v62, v63
	v_cvt_pk_fp8_f32 v71, v58, v59
	v_pk_mul_f32 v[64:65], v[64:65], v[74:75]
	v_pk_mul_f32 v[60:61], v[60:61], v[76:77]
	v_pk_mul_f32 v[64:65], v[64:65], s[20:21] op_sel_hi:[1,0]
	v_pk_mul_f32 v[60:61], v[60:61], s[20:21] op_sel_hi:[1,0]
	v_med3_f32 v64, v64, s54, v170
	v_med3_f32 v60, v60, s54, v170
	v_med3_f32 v58, v65, s54, v170
	v_med3_f32 v59, v61, s54, v170
	v_cvt_pk_fp8_f32 v70, v64, v58 op_sel:[0,0,1]
	v_cvt_pk_fp8_f32 v71, v60, v59 op_sel:[0,0,1]
	v_lshl_add_u64 v[60:61], s[10:11], 0, v[72:73]
	v_lshl_add_u64 v[62:63], v[60:61], 0, v[130:131]
	v_lshl_add_u64 v[58:59], v[84:85], 0, s[18:19]
	global_load_dwordx4 v[58:61], v[58:59], off offset:256
	global_store_dwordx2 v[62:63], v[70:71], off
	v_mov_b32_e32 v64, 0
	v_mov_b32_e32 v65, 0
	v_add_u32_e32 v66, 0x90, v132
	v_mad_i64_i32 v[68:69], s[24:25], v66, s50, v[134:135]
	v_lshl_add_u64 v[68:69], v[68:69], 0, v[136:137]
	s_waitcnt vmcnt(1)
	v_lshlrev_b32_e32 v67, 16, v58
	v_and_b32_e32 v58, 0xffff0000, v58
	v_lshlrev_b32_e32 v71, 16, v60
	v_and_b32_e32 v60, 0xffff0000, v60
	v_lshlrev_b32_e32 v70, 16, v59
	v_and_b32_e32 v59, 0xffff0000, v59
	v_lshlrev_b32_e32 v72, 16, v61
	v_and_b32_e32 v61, 0xffff0000, v61
	v_max_f32_e32 v67, v67, v67
	v_max_f32_e32 v71, v71, v71
	v_max_f32_e32 v73, v58, v58
	v_max_f32_e32 v74, v60, v60
	v_max_f32_e32 v75, v59, v59
	v_max_f32_e32 v76, v61, v61
	v_max_f32_e32 v58, 0xda24260, v67
	v_max_f32_e32 v60, 0xda24260, v71
	v_max_f32_e32 v59, 0xda24260, v73
	v_max_f32_e32 v61, 0xda24260, v74
	v_pk_mul_f32 v[50:51], v[50:51], v[58:59]
	v_pk_mul_f32 v[54:55], v[54:55], v[60:61]
	v_pk_mul_f32 v[50:51], v[50:51], s[20:21] op_sel_hi:[1,0]
	v_pk_mul_f32 v[54:55], v[54:55], s[20:21] op_sel_hi:[1,0]
	v_max_f32_e32 v70, v70, v70
	v_max_f32_e32 v72, v72, v72
	v_med3_f32 v50, v50, s54, v170
	v_med3_f32 v54, v54, s54, v170
	v_med3_f32 v51, v51, s54, v170
	v_med3_f32 v55, v55, s54, v170
	v_max_f32_e32 v70, 0xda24260, v70
	v_max_f32_e32 v72, 0xda24260, v72
	v_max_f32_e32 v71, 0xda24260, v75
	v_max_f32_e32 v73, 0xda24260, v76
	v_cvt_pk_fp8_f32 v64, v50, v51
	v_cvt_pk_fp8_f32 v65, v54, v55
	v_pk_mul_f32 v[52:53], v[52:53], v[70:71]
	v_pk_mul_f32 v[56:57], v[56:57], v[72:73]
	v_pk_mul_f32 v[52:53], v[52:53], s[20:21] op_sel_hi:[1,0]
	v_pk_mul_f32 v[56:57], v[56:57], s[20:21] op_sel_hi:[1,0]
	v_med3_f32 v52, v52, s54, v170
	v_med3_f32 v56, v56, s54, v170
	v_med3_f32 v50, v53, s54, v170
	v_med3_f32 v51, v57, s54, v170
	v_cvt_pk_fp8_f32 v64, v52, v50 op_sel:[0,0,1]
	v_cvt_pk_fp8_f32 v65, v56, v51 op_sel:[0,0,1]
	v_add_co_u32_e32 v50, vcc, s44, v68
	v_mov_b32_e32 v54, 0
	s_nop 0
	v_addc_co_u32_e32 v51, vcc, 0, v69, vcc
	global_load_dwordx4 v[50:53], v[50:51], off offset:3072
	global_store_dwordx2 v[62:63], v[64:65], off offset:128
	v_mov_b32_e32 v55, 0
	v_ashrrev_i32_e32 v67, 31, v66
	v_lshlrev_b64 v[56:57], 11, v[66:67]
	s_waitcnt vmcnt(1)
	v_lshlrev_b32_e32 v58, 16, v50
	v_and_b32_e32 v50, 0xffff0000, v50
	v_lshlrev_b32_e32 v60, 16, v52
	v_and_b32_e32 v52, 0xffff0000, v52
	v_lshlrev_b32_e32 v59, 16, v51
	v_and_b32_e32 v51, 0xffff0000, v51
	v_lshlrev_b32_e32 v61, 16, v53
	v_and_b32_e32 v53, 0xffff0000, v53
	v_max_f32_e32 v58, v58, v58
	v_max_f32_e32 v60, v60, v60
	v_max_f32_e32 v62, v50, v50
	v_max_f32_e32 v63, v52, v52
	v_max_f32_e32 v64, v51, v51
	v_max_f32_e32 v65, v53, v53
	v_max_f32_e32 v50, 0xda24260, v58
	v_max_f32_e32 v52, 0xda24260, v60
	v_max_f32_e32 v51, 0xda24260, v62
	v_max_f32_e32 v53, 0xda24260, v63
	v_pk_mul_f32 v[46:47], v[46:47], v[50:51]
	v_pk_mul_f32 v[42:43], v[42:43], v[52:53]
	v_pk_mul_f32 v[46:47], v[46:47], s[20:21] op_sel_hi:[1,0]
	v_pk_mul_f32 v[42:43], v[42:43], s[20:21] op_sel_hi:[1,0]
	v_max_f32_e32 v59, v59, v59
	v_max_f32_e32 v61, v61, v61
	v_med3_f32 v46, v46, s54, v170
	v_med3_f32 v42, v42, s54, v170
	v_med3_f32 v47, v47, s54, v170
	v_med3_f32 v43, v43, s54, v170
	v_max_f32_e32 v58, 0xda24260, v59
	v_max_f32_e32 v60, 0xda24260, v61
	v_max_f32_e32 v59, 0xda24260, v64
	v_max_f32_e32 v61, 0xda24260, v65
	v_cvt_pk_fp8_f32 v54, v46, v47
	v_cvt_pk_fp8_f32 v55, v42, v43
	v_pk_mul_f32 v[48:49], v[48:49], v[58:59]
	v_pk_mul_f32 v[44:45], v[44:45], v[60:61]
	v_pk_mul_f32 v[48:49], v[48:49], s[20:21] op_sel_hi:[1,0]
	v_pk_mul_f32 v[44:45], v[44:45], s[20:21] op_sel_hi:[1,0]
	v_med3_f32 v48, v48, s54, v170
	v_med3_f32 v44, v44, s54, v170
	v_med3_f32 v42, v49, s54, v170
	v_med3_f32 v43, v45, s54, v170
	v_cvt_pk_fp8_f32 v54, v48, v42 op_sel:[0,0,1]
	v_cvt_pk_fp8_f32 v55, v44, v43 op_sel:[0,0,1]
	v_lshl_add_u64 v[44:45], s[10:11], 0, v[56:57]
	v_lshl_add_u64 v[46:47], v[44:45], 0, v[130:131]
	v_lshl_add_u64 v[42:43], v[68:69], 0, s[18:19]
	global_load_dwordx4 v[42:45], v[42:43], off offset:256
	global_store_dwordx2 v[46:47], v[54:55], off
	v_mov_b32_e32 v48, 0
	v_mov_b32_e32 v49, 0
	v_add_u32_e32 v50, 0xa0, v132
	v_mad_i64_i32 v[52:53], s[24:25], v50, s50, v[134:135]
	v_lshl_add_u64 v[52:53], v[52:53], 0, v[136:137]
	s_waitcnt vmcnt(1)
	v_lshlrev_b32_e32 v51, 16, v42
	v_and_b32_e32 v42, 0xffff0000, v42
	v_lshlrev_b32_e32 v55, 16, v44
	v_and_b32_e32 v44, 0xffff0000, v44
	v_lshlrev_b32_e32 v54, 16, v43
	v_and_b32_e32 v43, 0xffff0000, v43
	v_lshlrev_b32_e32 v56, 16, v45
	v_and_b32_e32 v45, 0xffff0000, v45
	v_max_f32_e32 v51, v51, v51
	v_max_f32_e32 v55, v55, v55
	v_max_f32_e32 v57, v42, v42
	v_max_f32_e32 v58, v44, v44
	v_max_f32_e32 v59, v43, v43
	v_max_f32_e32 v60, v45, v45
	v_max_f32_e32 v42, 0xda24260, v51
	v_max_f32_e32 v44, 0xda24260, v55
	v_max_f32_e32 v43, 0xda24260, v57
	v_max_f32_e32 v45, 0xda24260, v58
	v_pk_mul_f32 v[34:35], v[34:35], v[42:43]
	v_pk_mul_f32 v[38:39], v[38:39], v[44:45]
	v_pk_mul_f32 v[34:35], v[34:35], s[20:21] op_sel_hi:[1,0]
	v_pk_mul_f32 v[38:39], v[38:39], s[20:21] op_sel_hi:[1,0]
	v_max_f32_e32 v54, v54, v54
	v_max_f32_e32 v56, v56, v56
	v_med3_f32 v34, v34, s54, v170
	v_med3_f32 v38, v38, s54, v170
	v_med3_f32 v35, v35, s54, v170
	v_med3_f32 v39, v39, s54, v170
	v_max_f32_e32 v54, 0xda24260, v54
	v_max_f32_e32 v56, 0xda24260, v56
	v_max_f32_e32 v55, 0xda24260, v59
	v_max_f32_e32 v57, 0xda24260, v60
	v_cvt_pk_fp8_f32 v48, v34, v35
	v_cvt_pk_fp8_f32 v49, v38, v39
	v_pk_mul_f32 v[36:37], v[36:37], v[54:55]
	v_pk_mul_f32 v[40:41], v[40:41], v[56:57]
	v_pk_mul_f32 v[36:37], v[36:37], s[20:21] op_sel_hi:[1,0]
	v_pk_mul_f32 v[40:41], v[40:41], s[20:21] op_sel_hi:[1,0]
	v_med3_f32 v36, v36, s54, v170
	v_med3_f32 v40, v40, s54, v170
	v_med3_f32 v34, v37, s54, v170
	v_med3_f32 v35, v41, s54, v170
	v_cvt_pk_fp8_f32 v48, v36, v34 op_sel:[0,0,1]
	v_cvt_pk_fp8_f32 v49, v40, v35 op_sel:[0,0,1]
	v_add_co_u32_e32 v34, vcc, s44, v52
	v_mov_b32_e32 v38, 0
	s_nop 0
	v_addc_co_u32_e32 v35, vcc, 0, v53, vcc
	global_load_dwordx4 v[34:37], v[34:35], off offset:3072
	global_store_dwordx2 v[46:47], v[48:49], off offset:128
	v_mov_b32_e32 v39, 0
	v_ashrrev_i32_e32 v51, 31, v50
	v_lshlrev_b64 v[40:41], 11, v[50:51]
	s_waitcnt vmcnt(1)
	v_lshlrev_b32_e32 v42, 16, v34
	v_and_b32_e32 v34, 0xffff0000, v34
	v_lshlrev_b32_e32 v44, 16, v36
	v_and_b32_e32 v36, 0xffff0000, v36
	v_lshlrev_b32_e32 v43, 16, v35
	v_and_b32_e32 v35, 0xffff0000, v35
	v_lshlrev_b32_e32 v45, 16, v37
	v_and_b32_e32 v37, 0xffff0000, v37
	v_max_f32_e32 v42, v42, v42
	v_max_f32_e32 v44, v44, v44
	v_max_f32_e32 v46, v34, v34
	v_max_f32_e32 v47, v36, v36
	v_max_f32_e32 v48, v35, v35
	v_max_f32_e32 v49, v37, v37
	v_max_f32_e32 v34, 0xda24260, v42
	v_max_f32_e32 v36, 0xda24260, v44
	v_max_f32_e32 v35, 0xda24260, v46
	v_max_f32_e32 v37, 0xda24260, v47
	v_pk_mul_f32 v[30:31], v[30:31], v[34:35]
	v_pk_mul_f32 v[26:27], v[26:27], v[36:37]
	v_pk_mul_f32 v[30:31], v[30:31], s[20:21] op_sel_hi:[1,0]
	v_pk_mul_f32 v[26:27], v[26:27], s[20:21] op_sel_hi:[1,0]
	v_max_f32_e32 v43, v43, v43
	v_max_f32_e32 v45, v45, v45
	v_med3_f32 v30, v30, s54, v170
	v_med3_f32 v26, v26, s54, v170
	v_med3_f32 v31, v31, s54, v170
	v_med3_f32 v27, v27, s54, v170
	v_max_f32_e32 v42, 0xda24260, v43
	v_max_f32_e32 v44, 0xda24260, v45
	v_max_f32_e32 v43, 0xda24260, v48
	v_max_f32_e32 v45, 0xda24260, v49
	v_cvt_pk_fp8_f32 v38, v30, v31
	v_cvt_pk_fp8_f32 v39, v26, v27
	v_pk_mul_f32 v[32:33], v[32:33], v[42:43]
	v_pk_mul_f32 v[28:29], v[28:29], v[44:45]
	v_pk_mul_f32 v[32:33], v[32:33], s[20:21] op_sel_hi:[1,0]
	v_pk_mul_f32 v[28:29], v[28:29], s[20:21] op_sel_hi:[1,0]
	v_med3_f32 v32, v32, s54, v170
	v_med3_f32 v28, v28, s54, v170
	v_med3_f32 v26, v33, s54, v170
	v_med3_f32 v27, v29, s54, v170
	v_cvt_pk_fp8_f32 v38, v32, v26 op_sel:[0,0,1]
	v_cvt_pk_fp8_f32 v39, v28, v27 op_sel:[0,0,1]
	v_lshl_add_u64 v[28:29], s[10:11], 0, v[40:41]
	v_lshl_add_u64 v[30:31], v[28:29], 0, v[130:131]
	v_lshl_add_u64 v[26:27], v[52:53], 0, s[18:19]
	global_load_dwordx4 v[26:29], v[26:27], off offset:256
	global_store_dwordx2 v[30:31], v[38:39], off
	v_mov_b32_e32 v32, 0
	v_mov_b32_e32 v33, 0
	v_add_u32_e32 v34, 0xb0, v132
	v_mad_i64_i32 v[36:37], s[24:25], v34, s50, v[134:135]
	v_lshl_add_u64 v[36:37], v[36:37], 0, v[136:137]
	s_waitcnt vmcnt(1)
	v_lshlrev_b32_e32 v35, 16, v26
	v_and_b32_e32 v26, 0xffff0000, v26
	v_lshlrev_b32_e32 v39, 16, v28
	v_and_b32_e32 v28, 0xffff0000, v28
	v_lshlrev_b32_e32 v38, 16, v27
	v_and_b32_e32 v27, 0xffff0000, v27
	v_lshlrev_b32_e32 v40, 16, v29
	v_and_b32_e32 v29, 0xffff0000, v29
	v_max_f32_e32 v35, v35, v35
	v_max_f32_e32 v39, v39, v39
	v_max_f32_e32 v41, v26, v26
	v_max_f32_e32 v42, v28, v28
	v_max_f32_e32 v43, v27, v27
	v_max_f32_e32 v44, v29, v29
	v_max_f32_e32 v26, 0xda24260, v35
	v_max_f32_e32 v28, 0xda24260, v39
	v_max_f32_e32 v27, 0xda24260, v41
	v_max_f32_e32 v29, 0xda24260, v42
	v_pk_mul_f32 v[18:19], v[18:19], v[26:27]
	v_pk_mul_f32 v[22:23], v[22:23], v[28:29]
	v_pk_mul_f32 v[18:19], v[18:19], s[20:21] op_sel_hi:[1,0]
	v_pk_mul_f32 v[22:23], v[22:23], s[20:21] op_sel_hi:[1,0]
	v_max_f32_e32 v38, v38, v38
	v_max_f32_e32 v40, v40, v40
	v_med3_f32 v18, v18, s54, v170
	v_med3_f32 v22, v22, s54, v170
	v_med3_f32 v19, v19, s54, v170
	v_med3_f32 v23, v23, s54, v170
	v_max_f32_e32 v38, 0xda24260, v38
	v_max_f32_e32 v40, 0xda24260, v40
	v_max_f32_e32 v39, 0xda24260, v43
	v_max_f32_e32 v41, 0xda24260, v44
	v_cvt_pk_fp8_f32 v32, v18, v19
	v_cvt_pk_fp8_f32 v33, v22, v23
	v_pk_mul_f32 v[20:21], v[20:21], v[38:39]
	v_pk_mul_f32 v[24:25], v[24:25], v[40:41]
	v_pk_mul_f32 v[20:21], v[20:21], s[20:21] op_sel_hi:[1,0]
	v_pk_mul_f32 v[24:25], v[24:25], s[20:21] op_sel_hi:[1,0]
	v_med3_f32 v20, v20, s54, v170
	v_med3_f32 v24, v24, s54, v170
	v_med3_f32 v18, v21, s54, v170
	v_med3_f32 v19, v25, s54, v170
	v_cvt_pk_fp8_f32 v32, v20, v18 op_sel:[0,0,1]
	v_cvt_pk_fp8_f32 v33, v24, v19 op_sel:[0,0,1]
	v_add_co_u32_e32 v18, vcc, s44, v36
	v_mov_b32_e32 v22, 0
	s_nop 0
	v_addc_co_u32_e32 v19, vcc, 0, v37, vcc
	global_load_dwordx4 v[18:21], v[18:19], off offset:3072
	global_store_dwordx2 v[30:31], v[32:33], off offset:128
	v_mov_b32_e32 v23, 0
	v_ashrrev_i32_e32 v35, 31, v34
	v_lshlrev_b64 v[24:25], 11, v[34:35]
	s_and_b64 vcc, exec, s[0:1]
	s_mov_b64 s[0:1], -1
	s_waitcnt vmcnt(1)
	v_lshlrev_b32_e32 v26, 16, v18
	v_and_b32_e32 v18, 0xffff0000, v18
	v_lshlrev_b32_e32 v28, 16, v20
	v_and_b32_e32 v20, 0xffff0000, v20
	v_lshlrev_b32_e32 v27, 16, v19
	v_and_b32_e32 v19, 0xffff0000, v19
	v_lshlrev_b32_e32 v29, 16, v21
	v_and_b32_e32 v21, 0xffff0000, v21
	v_max_f32_e32 v26, v26, v26
	v_max_f32_e32 v28, v28, v28
	v_max_f32_e32 v30, v18, v18
	v_max_f32_e32 v31, v20, v20
	v_max_f32_e32 v32, v19, v19
	v_max_f32_e32 v33, v21, v21
	v_max_f32_e32 v18, 0xda24260, v26
	v_max_f32_e32 v20, 0xda24260, v28
	v_max_f32_e32 v19, 0xda24260, v30
	v_max_f32_e32 v21, 0xda24260, v31
	v_pk_mul_f32 v[6:7], v[6:7], v[18:19]
	v_pk_mul_f32 v[2:3], v[2:3], v[20:21]
	v_pk_mul_f32 v[6:7], v[6:7], s[20:21] op_sel_hi:[1,0]
	v_pk_mul_f32 v[2:3], v[2:3], s[20:21] op_sel_hi:[1,0]
	v_max_f32_e32 v27, v27, v27
	v_max_f32_e32 v29, v29, v29
	v_med3_f32 v6, v6, s54, v170
	v_med3_f32 v2, v2, s54, v170
	v_med3_f32 v7, v7, s54, v170
	v_med3_f32 v3, v3, s54, v170
	v_max_f32_e32 v26, 0xda24260, v27
	v_max_f32_e32 v28, 0xda24260, v29
	v_max_f32_e32 v27, 0xda24260, v32
	v_max_f32_e32 v29, 0xda24260, v33
	v_cvt_pk_fp8_f32 v22, v6, v7
	v_cvt_pk_fp8_f32 v23, v2, v3
	v_pk_mul_f32 v[8:9], v[8:9], v[26:27]
	v_pk_mul_f32 v[4:5], v[4:5], v[28:29]
	v_pk_mul_f32 v[8:9], v[8:9], s[20:21] op_sel_hi:[1,0]
	v_pk_mul_f32 v[4:5], v[4:5], s[20:21] op_sel_hi:[1,0]
	v_med3_f32 v8, v8, s54, v170
	v_med3_f32 v4, v4, s54, v170
	v_med3_f32 v2, v9, s54, v170
	v_med3_f32 v3, v5, s54, v170
	v_cvt_pk_fp8_f32 v22, v8, v2 op_sel:[0,0,1]
	v_cvt_pk_fp8_f32 v23, v4, v3 op_sel:[0,0,1]
	v_lshl_add_u64 v[4:5], s[10:11], 0, v[24:25]
	v_lshl_add_u64 v[6:7], v[4:5], 0, v[130:131]
	v_lshl_add_u64 v[2:3], v[36:37], 0, s[18:19]
	global_load_dwordx4 v[2:5], v[2:3], off offset:256
	global_store_dwordx2 v[6:7], v[22:23], off
	v_mov_b32_e32 v8, 0
	v_mov_b32_e32 v9, 0
	s_waitcnt vmcnt(1)
	v_lshlrev_b32_e32 v18, 16, v2
	v_and_b32_e32 v2, 0xffff0000, v2
	v_lshlrev_b32_e32 v20, 16, v4
	v_and_b32_e32 v4, 0xffff0000, v4
	v_lshlrev_b32_e32 v19, 16, v3
	v_and_b32_e32 v3, 0xffff0000, v3
	v_lshlrev_b32_e32 v21, 16, v5
	v_and_b32_e32 v5, 0xffff0000, v5
	v_max_f32_e32 v18, v18, v18
	v_max_f32_e32 v20, v20, v20
	v_max_f32_e32 v22, v2, v2
	v_max_f32_e32 v23, v4, v4
	v_max_f32_e32 v24, v3, v3
	v_max_f32_e32 v25, v5, v5
	v_max_f32_e32 v2, 0xda24260, v18
	v_max_f32_e32 v4, 0xda24260, v20
	v_max_f32_e32 v3, 0xda24260, v22
	v_max_f32_e32 v5, 0xda24260, v23
	v_pk_mul_f32 v[2:3], v[10:11], v[2:3]
	v_pk_mul_f32 v[4:5], v[14:15], v[4:5]
	v_pk_mul_f32 v[2:3], v[2:3], s[20:21] op_sel_hi:[1,0]
	v_pk_mul_f32 v[4:5], v[4:5], s[20:21] op_sel_hi:[1,0]
	v_max_f32_e32 v19, v19, v19
	v_max_f32_e32 v21, v21, v21
	v_med3_f32 v2, v2, s54, v170
	v_med3_f32 v4, v4, s54, v170
	v_med3_f32 v3, v3, s54, v170
	v_med3_f32 v5, v5, s54, v170
	v_max_f32_e32 v18, 0xda24260, v19
	v_max_f32_e32 v20, 0xda24260, v21
	v_max_f32_e32 v19, 0xda24260, v24
	v_max_f32_e32 v21, 0xda24260, v25
	v_cvt_pk_fp8_f32 v8, v2, v3
	v_cvt_pk_fp8_f32 v9, v4, v5
	v_pk_mul_f32 v[10:11], v[12:13], v[18:19]
	v_pk_mul_f32 v[12:13], v[16:17], v[20:21]
	v_pk_mul_f32 v[10:11], v[10:11], s[20:21] op_sel_hi:[1,0]
	v_pk_mul_f32 v[12:13], v[12:13], s[20:21] op_sel_hi:[1,0]
	v_med3_f32 v10, v10, s54, v170
	v_med3_f32 v12, v12, s54, v170
	v_med3_f32 v2, v11, s54, v170
	v_med3_f32 v3, v13, s54, v170
	v_cvt_pk_fp8_f32 v8, v10, v2 op_sel:[0,0,1]
	v_cvt_pk_fp8_f32 v9, v12, v3 op_sel:[0,0,1]
	global_store_dwordx2 v[6:7], v[8:9], off offset:128
	s_cbranch_vccnz .LBB0_664
	s_andn2_b64 vcc, exec, s[6:7]
	s_cbranch_vccnz .LBB0_663
	s_barrier
	s_branch .LBB0_663
